# stats2: short-path branch taken before the slot 4/5 masks are computed (shorter branch chain on the common path)
# speedup vs baseline: 1.0015x; 1.0015x over previous
_Z13stats2_kernelPKiS0_PKfS2_S0_P15HIP_vector_typeIfLj4EEi:
	s_load_dwordx8 s[4:11], s[0:1], 0x0
	s_load_dwordx4 s[12:15], s[0:1], 0x20
	s_load_dword s16, s[0:1], 0x30
	v_lshrrev_b32_e32 v1, 3, v0
	v_lshl_or_b32 v1, s2, 5, v1
	v_and_b32_e32 v2, 7, v0
	v_mov_b32_e32 v25, 0xff800000
	s_waitcnt lgkmcnt(0)
	s_add_i32 s17, s16, -1
	v_cmp_gt_i32_e64 s[18:19], s16, v1
	v_min_i32_e32 v1, s17, v1
	v_lshlrev_b32_e32 v3, 2, v1
	global_load_dword v4, v3, s[4:5]
	global_load_dword v5, v3, s[4:5] offset:4
	global_load_dword v6, v3, s[10:11]
	global_load_dword v7, v3, s[8:9]
	global_load_dword v8, v3, s[12:13]
	s_waitcnt vmcnt(3)
	v_sub_u32_e32 v5, v5, v4
	v_add_u32_e32 v9, v4, v2
	v_lshlrev_b32_e32 v9, 2, v9
	v_cmp_lt_i32_e64 s[20:21], v2, v5
	v_add_u32_e32 v23, 8, v2
	v_cmp_lt_i32_e64 s[22:23], v23, v5
	v_add_u32_e32 v23, 16, v2
	v_cmp_lt_i32_e64 s[24:25], v23, v5
	v_add_u32_e32 v23, 24, v2
	v_cmp_lt_i32_e64 s[26:27], v23, v5
	s_cmp_eq_u64 s[26:27], 0
	s_cbranch_scc1 .Lst2_short
	v_add_u32_e32 v23, 32, v2
	v_cmp_lt_i32_e64 s[28:29], v23, v5
	v_add_u32_e32 v23, 40, v2
	v_cmp_lt_i32_e64 s[30:31], v23, v5
	s_mov_b64 exec, s[20:21]
	global_load_dword v10, v9, s[6:7]
	s_mov_b64 exec, s[22:23]
	global_load_dword v11, v9, s[6:7] offset:32
	s_mov_b64 exec, s[24:25]
	global_load_dword v12, v9, s[6:7] offset:64
	s_mov_b64 exec, s[26:27]
	global_load_dword v13, v9, s[6:7] offset:96
	s_mov_b64 exec, s[28:29]
	global_load_dword v14, v9, s[6:7] offset:128
	s_mov_b64 exec, s[30:31]
	global_load_dword v15, v9, s[6:7] offset:160
	s_mov_b64 exec, -1
	s_waitcnt vmcnt(0)
	s_mov_b64 exec, s[20:21]
	v_lshlrev_b32_e32 v10, 2, v10
	global_load_dword v10, v10, s[8:9]
	s_mov_b64 exec, s[22:23]
	v_lshlrev_b32_e32 v11, 2, v11
	global_load_dword v11, v11, s[8:9]
	s_mov_b64 exec, s[24:25]
	v_lshlrev_b32_e32 v12, 2, v12
	global_load_dword v12, v12, s[8:9]
	s_mov_b64 exec, s[26:27]
	v_lshlrev_b32_e32 v13, 2, v13
	global_load_dword v13, v13, s[8:9]
	s_mov_b64 exec, s[28:29]
	v_lshlrev_b32_e32 v14, 2, v14
	global_load_dword v14, v14, s[8:9]
	s_mov_b64 exec, s[30:31]
	v_lshlrev_b32_e32 v15, 2, v15
	global_load_dword v15, v15, s[8:9]
	s_mov_b64 exec, -1
	v_add_f32_e32 v22, v6, v7
	v_mul_f32_e32 v23, 0x3e4ccccd, v22
	v_max_f32_e32 v22, v22, v23
	s_waitcnt vmcnt(0)
	v_add_f32_e32 v16, v6, v10
	v_mul_f32_e32 v23, 0x3e4ccccd, v16
	v_max_f32_e32 v16, v16, v23
	v_cndmask_b32_e64 v16, v25, v16, s[20:21]
	v_add_f32_e32 v17, v6, v11
	v_mul_f32_e32 v23, 0x3e4ccccd, v17
	v_max_f32_e32 v17, v17, v23
	v_cndmask_b32_e64 v17, v25, v17, s[22:23]
	v_add_f32_e32 v18, v6, v12
	v_mul_f32_e32 v23, 0x3e4ccccd, v18
	v_max_f32_e32 v18, v18, v23
	v_cndmask_b32_e64 v18, v25, v18, s[24:25]
	v_add_f32_e32 v19, v6, v13
	v_mul_f32_e32 v23, 0x3e4ccccd, v19
	v_max_f32_e32 v19, v19, v23
	v_cndmask_b32_e64 v19, v25, v19, s[26:27]
	v_add_f32_e32 v20, v6, v14
	v_mul_f32_e32 v23, 0x3e4ccccd, v20
	v_max_f32_e32 v20, v20, v23
	v_cndmask_b32_e64 v20, v25, v20, s[28:29]
	v_add_f32_e32 v21, v6, v15
	v_mul_f32_e32 v23, 0x3e4ccccd, v21
	v_max_f32_e32 v21, v21, v23
	v_cndmask_b32_e64 v21, v25, v21, s[30:31]
	v_max3_f32 v24, v22, v16, v17
	v_max3_f32 v24, v24, v18, v19
	v_max3_f32 v24, v24, v20, v21
	v_add_u32_e32 v26, 48, v2
	v_add_u32_e32 v27, 192, v9
